# v11_p3merge
# speedup vs baseline: 1.0158x; 1.0042x over previous
.LBB1_123:
	s_add_i32 s99, s54, s98
	s_lshr_b32 vcc_lo, s99, 2
	s_add_i32 s99, s99, vcc_lo
	s_and_b32 s99, s99, 3
	s_cmp_lg_u32 s99, s86
	s_cbranch_scc1 .LBB1_122
	ds_read2_b32 v[70:71], v68 offset1:4
	ds_read2_b32 v[166:167], v68 offset0:8 offset1:12
	v_add_u32_e32 v72, s97, v67
	v_add_u32_e32 v73, 0x1ed00, v69
	ds_read2_b32 a[0:1], v72 offset1:68
	ds_read2_b32 a[2:3], v72 offset0:136 offset1:204
	ds_read_b32 v73, v73
	v_add_u32_e32 v163, 0x1ed10, v69
	v_add_u32_e32 v164, 0x1ed20, v69
	v_add_u32_e32 v165, 0x1ed30, v69
	ds_read_b32 v163, v163
	ds_read_b32 v164, v164
	ds_read_b32 v165, v165
	s_waitcnt lgkmcnt(0)
	v_xor_b32_e32 v70, 0x80000000, v70
	v_xor_b32_e32 v71, 0x80000000, v71
	v_xor_b32_e32 v166, 0x80000000, v166
	v_xor_b32_e32 v167, 0x80000000, v167
	v_mfma_f32_16x16x4_f32 a[0:3], v70, v73, a[0:3]
	v_mfma_f32_16x16x4_f32 a[0:3], v71, v163, a[0:3]
	v_mfma_f32_16x16x4_f32 a[0:3], v166, v164, a[0:3]
	v_mfma_f32_16x16x4_f32 a[0:3], v167, v165, a[0:3]
	s_nop 9
	ds_write_b32 v72, a0
	ds_write_b32 v72, a1 offset:272
	ds_write_b32 v72, a2 offset:544
	ds_write_b32 v72, a3 offset:816
	s_branch .LBB1_122

.LBB1_244:
	s_add_i32 s99, s52, s98
	s_lshr_b32 vcc_lo, s99, 2
	s_add_i32 s99, s99, vcc_lo
	s_and_b32 s99, s99, 3
	s_cmp_lg_u32 s99, s86
	s_cbranch_scc1 .LBB1_243
	ds_read2_b32 v[6:7], v4 offset1:4
	ds_read2_b32 v[16:17], v4 offset0:8 offset1:12
	v_add_u32_e32 v8, s97, v3
	v_add_u32_e32 v9, 0x1a900, v5
	ds_read2_b32 a[0:1], v8 offset1:68
	ds_read2_b32 a[2:3], v8 offset0:136 offset1:204
	ds_read_b32 v9, v9
	v_add_u32_e32 v13, 0x1a910, v5
	v_add_u32_e32 v14, 0x1a920, v5
	v_add_u32_e32 v15, 0x1a930, v5
	ds_read_b32 v13, v13
	ds_read_b32 v14, v14
	ds_read_b32 v15, v15
	s_waitcnt lgkmcnt(0)
	v_xor_b32_e32 v6, 0x80000000, v6
	v_xor_b32_e32 v7, 0x80000000, v7
	v_xor_b32_e32 v16, 0x80000000, v16
	v_xor_b32_e32 v17, 0x80000000, v17
	v_mfma_f32_16x16x4_f32 a[0:3], v6, v9, a[0:3]
	v_mfma_f32_16x16x4_f32 a[0:3], v7, v13, a[0:3]
	v_mfma_f32_16x16x4_f32 a[0:3], v16, v14, a[0:3]
	v_mfma_f32_16x16x4_f32 a[0:3], v17, v15, a[0:3]
	s_nop 9
	ds_write_b32 v8, a0
	ds_write_b32 v8, a1 offset:272
	ds_write_b32 v8, a2 offset:544
	ds_write_b32 v8, a3 offset:816
	s_branch .LBB1_243

.LBB1_314:
	s_add_i32 s83, s53, s82
	s_lshr_b32 vcc_lo, s83, 2
	s_add_i32 s83, s83, vcc_lo
	s_and_b32 s83, s83, 3
	s_cmp_lg_u32 s83, s86
	s_cbranch_scc1 .LBB1_313
	ds_read2_b32 v[6:7], v4 offset1:4
	ds_read2_b32 v[54:55], v4 offset0:8 offset1:12
	v_add_u32_e32 v8, s81, v3
	v_add_u32_e32 v9, 0x1ed00, v5
	ds_read2_b32 a[0:1], v8 offset1:68
	ds_read2_b32 a[2:3], v8 offset0:136 offset1:204
	ds_read_b32 v9, v9
	v_add_u32_e32 v41, 0x1ed10, v5
	v_add_u32_e32 v42, 0x1ed20, v5
	v_add_u32_e32 v44, 0x1ed30, v5
	ds_read_b32 v41, v41
	ds_read_b32 v42, v42
	ds_read_b32 v44, v44
	s_waitcnt lgkmcnt(0)
	v_xor_b32_e32 v6, 0x80000000, v6
	v_xor_b32_e32 v7, 0x80000000, v7
	v_xor_b32_e32 v54, 0x80000000, v54
	v_xor_b32_e32 v55, 0x80000000, v55
	v_mfma_f32_16x16x4_f32 a[0:3], v6, v9, a[0:3]
	v_mfma_f32_16x16x4_f32 a[0:3], v7, v41, a[0:3]
	v_mfma_f32_16x16x4_f32 a[0:3], v54, v42, a[0:3]
	v_mfma_f32_16x16x4_f32 a[0:3], v55, v44, a[0:3]
	s_nop 9
	ds_write_b32 v8, a0
	ds_write_b32 v8, a1 offset:272
	ds_write_b32 v8, a2 offset:544
	ds_write_b32 v8, a3 offset:816
	s_branch .LBB1_313

.LBB1_355:
	s_add_i32 s81, s53, s80
	s_lshr_b32 vcc_lo, s81, 2
	s_add_i32 s81, s81, vcc_lo
	s_and_b32 s81, s81, 3
	s_cmp_lg_u32 s81, s86
	s_cbranch_scc1 .LBB1_354
	ds_read2_b32 v[4:5], v2 offset1:4
	ds_read2_b32 v[36:37], v2 offset0:8 offset1:12
	v_add_u32_e32 v6, s79, v1
	v_add_u32_e32 v7, 0x1a900, v3
	ds_read2_b32 a[0:1], v6 offset1:68
	ds_read2_b32 a[2:3], v6 offset0:136 offset1:204
	ds_read_b32 v7, v7
	v_add_u32_e32 v14, 0x1a910, v3
	v_add_u32_e32 v34, 0x1a920, v3
	v_add_u32_e32 v35, 0x1a930, v3
	ds_read_b32 v14, v14
	ds_read_b32 v34, v34
	ds_read_b32 v35, v35
	s_waitcnt lgkmcnt(0)
	v_xor_b32_e32 v4, 0x80000000, v4
	v_xor_b32_e32 v5, 0x80000000, v5
	v_xor_b32_e32 v36, 0x80000000, v36
	v_xor_b32_e32 v37, 0x80000000, v37
	v_mfma_f32_16x16x4_f32 a[0:3], v4, v7, a[0:3]
	v_mfma_f32_16x16x4_f32 a[0:3], v5, v14, a[0:3]
	v_mfma_f32_16x16x4_f32 a[0:3], v36, v34, a[0:3]
	v_mfma_f32_16x16x4_f32 a[0:3], v37, v35, a[0:3]
	s_nop 9
	ds_write_b32 v6, a0
	ds_write_b32 v6, a1 offset:272
	ds_write_b32 v6, a2 offset:544
	ds_write_b32 v6, a3 offset:816
	s_branch .LBB1_354
